# speedup vs baseline: 1.0026x; 1.0026x over previous
.LBB1_46:
	s_load_dwordx2 s[0:1], s[0:1], 0x20
	s_and_b64 vcc, exec, s[20:21]
	s_waitcnt lgkmcnt(0)
	s_barrier
	s_cbranch_vccnz .LBB1_48
	s_waitcnt vmcnt(0)
	v_mul_u32_u24_e32 v0, 0x110, v26
	v_add_u32_e32 v15, v16, v0
	ds_read_b128 v[0:3], v15 offset:19040
	ds_read_b128 v[4:7], v12 offset:816
	ds_read_b128 v[18:21], v15 offset:19072
	ds_read_b128 v[8:11], v12 offset:848
	ds_read_b128 v[140:143], v15 offset:19104
	ds_read_b128 v[144:147], v12 offset:880
	ds_read_b128 v[148:151], v15 offset:19136
	ds_read_b128 v[152:155], v12 offset:912
	ds_read_b128 v[156:159], v15 offset:19168
	ds_read_b128 v[160:163], v12 offset:944
	ds_read_b128 v[164:167], v15 offset:19200
	ds_read_b128 v[168:171], v12 offset:976
	s_waitcnt lgkmcnt(10)
	v_mfma_f32_32x32x16_f16 a[0:15], v[0:3], v[4:7], a[0:15]
	s_waitcnt lgkmcnt(8)
	v_mfma_f32_32x32x16_f16 a[0:15], v[18:21], v[8:11], a[0:15]
	ds_read_b128 v[0:3], v15 offset:19232
	ds_read_b128 v[4:7], v12 offset:1008
	ds_read_b128 v[18:21], v15 offset:19264
	ds_read_b128 v[8:11], v12 offset:1040
	s_waitcnt lgkmcnt(10)
	v_mfma_f32_32x32x16_f16 a[0:15], v[140:143], v[144:147], a[0:15]
	s_waitcnt lgkmcnt(8)
	v_mfma_f32_32x32x16_f16 a[0:15], v[148:151], v[152:155], a[0:15]
	ds_read_b128 v[140:143], v15 offset:36448
	ds_read_b128 v[144:147], v13 offset:816
	ds_read_b128 v[148:151], v15 offset:36480
	ds_read_b128 v[152:155], v13 offset:848
	s_waitcnt lgkmcnt(10)
	v_mfma_f32_32x32x16_f16 a[0:15], v[156:159], v[160:163], a[0:15]
	s_waitcnt lgkmcnt(8)
	v_mfma_f32_32x32x16_f16 a[0:15], v[164:167], v[168:171], a[0:15]
	ds_read_b128 v[156:159], v15 offset:36512
	ds_read_b128 v[160:163], v13 offset:880
	ds_read_b128 v[164:167], v15 offset:36544
	ds_read_b128 v[168:171], v13 offset:912
	s_waitcnt lgkmcnt(10)
	v_mfma_f32_32x32x16_f16 a[0:15], v[0:3], v[4:7], a[0:15]
	s_waitcnt lgkmcnt(8)
	v_mfma_f32_32x32x16_f16 a[0:15], v[18:21], v[8:11], a[0:15]
	ds_read_b128 v[0:3], v15 offset:36576
	ds_read_b128 v[4:7], v13 offset:944
	ds_read_b128 v[18:21], v15 offset:36608
	ds_read_b128 v[8:11], v13 offset:976
	s_waitcnt lgkmcnt(10)
	v_mfma_f32_32x32x16_f16 a[0:15], v[140:143], v[144:147], a[0:15]
	s_waitcnt lgkmcnt(8)
	v_mfma_f32_32x32x16_f16 a[0:15], v[148:151], v[152:155], a[0:15]
	ds_read_b128 v[140:143], v15 offset:36640
	ds_read_b128 v[144:147], v13 offset:1008
	ds_read_b128 v[148:151], v15 offset:36672
	ds_read_b128 v[152:155], v13 offset:1040
	s_waitcnt lgkmcnt(10)
	v_mfma_f32_32x32x16_f16 a[0:15], v[156:159], v[160:163], a[0:15]
	s_waitcnt lgkmcnt(8)
	v_mfma_f32_32x32x16_f16 a[0:15], v[164:167], v[168:171], a[0:15]
	ds_read_b128 v[156:159], v15 offset:53856
	ds_read_b128 v[160:163], v14 offset:816
	ds_read_b128 v[164:167], v15 offset:53888
	ds_read_b128 v[168:171], v14 offset:848
	s_waitcnt lgkmcnt(10)
	v_mfma_f32_32x32x16_f16 a[0:15], v[0:3], v[4:7], a[0:15]
	s_waitcnt lgkmcnt(8)
	v_mfma_f32_32x32x16_f16 a[0:15], v[18:21], v[8:11], a[0:15]
	ds_read_b128 v[0:3], v15 offset:53920
	ds_read_b128 v[4:7], v14 offset:880
	ds_read_b128 v[18:21], v15 offset:53952
	ds_read_b128 v[8:11], v14 offset:912
	s_waitcnt lgkmcnt(10)
	v_mfma_f32_32x32x16_f16 a[0:15], v[140:143], v[144:147], a[0:15]
	s_waitcnt lgkmcnt(8)
	v_mfma_f32_32x32x16_f16 a[0:15], v[148:151], v[152:155], a[0:15]
	ds_read_b128 v[140:143], v15 offset:53984
	ds_read_b128 v[144:147], v14 offset:944
	ds_read_b128 v[148:151], v15 offset:54016
	ds_read_b128 v[152:155], v14 offset:976
	s_waitcnt lgkmcnt(10)
	v_mfma_f32_32x32x16_f16 a[0:15], v[156:159], v[160:163], a[0:15]
	s_waitcnt lgkmcnt(8)
	v_mfma_f32_32x32x16_f16 a[0:15], v[164:167], v[168:171], a[0:15]
	ds_read_b128 v[156:159], v15 offset:54048
	ds_read_b128 v[160:163], v14 offset:1008
	ds_read_b128 v[164:167], v15 offset:54080
	ds_read_b128 v[168:171], v14 offset:1040
	s_waitcnt lgkmcnt(10)
	v_mfma_f32_32x32x16_f16 a[0:15], v[0:3], v[4:7], a[0:15]
	s_waitcnt lgkmcnt(8)
	v_mfma_f32_32x32x16_f16 a[0:15], v[18:21], v[8:11], a[0:15]
	s_waitcnt lgkmcnt(6)
	v_mfma_f32_32x32x16_f16 a[0:15], v[140:143], v[144:147], a[0:15]
	s_waitcnt lgkmcnt(4)
	v_mfma_f32_32x32x16_f16 a[0:15], v[148:151], v[152:155], a[0:15]
	s_waitcnt lgkmcnt(2)
	v_mfma_f32_32x32x16_f16 a[0:15], v[156:159], v[160:163], a[0:15]
	s_waitcnt lgkmcnt(0)
	v_mfma_f32_32x32x16_f16 a[0:15], v[164:167], v[168:171], a[0:15]

	.amdhsa_kernel _Z9k_coarse2PKtS0_PKdS2_Pf
		.amdhsa_group_segment_fixed_size 256
		.amdhsa_private_segment_fixed_size 0
		.amdhsa_kernarg_size 40
		.amdhsa_user_sgpr_count 2
		.amdhsa_user_sgpr_dispatch_ptr 0
		.amdhsa_user_sgpr_queue_ptr 0
		.amdhsa_user_sgpr_kernarg_segment_ptr 1
		.amdhsa_user_sgpr_dispatch_id 0
		.amdhsa_user_sgpr_kernarg_preload_length 0
		.amdhsa_user_sgpr_kernarg_preload_offset 0
		.amdhsa_user_sgpr_private_segment_size 0
		.amdhsa_uses_dynamic_stack 0
		.amdhsa_enable_private_segment 0
		.amdhsa_system_sgpr_workgroup_id_x 1
		.amdhsa_system_sgpr_workgroup_id_y 0
		.amdhsa_system_sgpr_workgroup_id_z 0
		.amdhsa_system_sgpr_workgroup_info 0
		.amdhsa_system_vgpr_workitem_id 0
		.amdhsa_next_free_vgpr 188
		.amdhsa_next_free_sgpr 31
		.amdhsa_accum_offset 172
		.amdhsa_reserve_vcc 1
		.amdhsa_float_round_mode_32 0
		.amdhsa_float_round_mode_16_64 0
		.amdhsa_float_denorm_mode_32 3
		.amdhsa_float_denorm_mode_16_64 3
		.amdhsa_dx10_clamp 1
		.amdhsa_ieee_mode 1
		.amdhsa_fp16_overflow 0
		.amdhsa_tg_split 0
		.amdhsa_exception_fp_ieee_invalid_op 0
		.amdhsa_exception_fp_denorm_src 0
		.amdhsa_exception_fp_ieee_div_zero 0
		.amdhsa_exception_fp_ieee_overflow 0
		.amdhsa_exception_fp_ieee_underflow 0
		.amdhsa_exception_fp_ieee_inexact 0
		.amdhsa_exception_int_div_zero 0
	.end_amdhsa_kernel

amdhsa.kernels:
  - .agpr_count:     0
    .args:
      - .actual_access:  read_only
        .address_space:  global
        .offset:         0
        .size:           8
        .value_kind:     global_buffer
      - .actual_access:  read_only
        .address_space:  global
        .offset:         8
        .size:           8
        .value_kind:     global_buffer
      - .actual_access:  write_only
        .address_space:  global
        .offset:         16
        .size:           8
        .value_kind:     global_buffer
      - .actual_access:  write_only
        .address_space:  global
        .offset:         24
        .size:           8
        .value_kind:     global_buffer
      - .actual_access:  write_only
        .address_space:  global
        .offset:         32
        .size:           8
        .value_kind:     global_buffer
      - .actual_access:  write_only
        .address_space:  global
        .offset:         40
        .size:           8
        .value_kind:     global_buffer
      - .actual_access:  write_only
        .address_space:  global
        .offset:         48
        .size:           8
        .value_kind:     global_buffer
      - .actual_access:  write_only
        .address_space:  global
        .offset:         56
        .size:           8
        .value_kind:     global_buffer
      - .actual_access:  write_only
        .address_space:  global
        .offset:         64
        .size:           8
        .value_kind:     global_buffer
    .group_segment_fixed_size: 18944
    .kernarg_segment_align: 8
    .kernarg_segment_size: 72
    .language:       OpenCL C
    .language_version:
      - 2
      - 0
    .max_flat_workgroup_size: 256
    .name:           _Z6k_prepPKfS0_PfS1_PdS2_PtS3_S3_
    .private_segment_fixed_size: 0
    .sgpr_count:     34
    .sgpr_spill_count: 0
    .symbol:         _Z6k_prepPKfS0_PfS1_PdS2_PtS3_S3_.kd
    .uniform_work_group_size: 1
    .uses_dynamic_stack: false
    .vgpr_count:     29
    .vgpr_spill_count: 0
    .wavefront_size: 64
  - .agpr_count:     16
    .args:
      - .actual_access:  read_only
        .address_space:  global
        .offset:         0
        .size:           8
        .value_kind:     global_buffer
      - .actual_access:  read_only
        .address_space:  global
        .offset:         8
        .size:           8
        .value_kind:     global_buffer
      - .actual_access:  read_only
        .address_space:  global
        .offset:         16
        .size:           8
        .value_kind:     global_buffer
      - .actual_access:  read_only
        .address_space:  global
        .offset:         24
        .size:           8
        .value_kind:     global_buffer
      - .actual_access:  write_only
        .address_space:  global
        .offset:         32
        .size:           8
        .value_kind:     global_buffer
    .group_segment_fixed_size: 256
    .kernarg_segment_align: 8
    .kernarg_segment_size: 40
    .language:       OpenCL C
    .language_version:
      - 2
      - 0
    .max_flat_workgroup_size: 256
    .name:           _Z9k_coarse2PKtS0_PKdS2_Pf
    .private_segment_fixed_size: 0
    .sgpr_count:     37
    .sgpr_spill_count: 0
    .symbol:         _Z9k_coarse2PKtS0_PKdS2_Pf.kd
    .uniform_work_group_size: 1
    .uses_dynamic_stack: false
    .vgpr_count:     188
    .vgpr_spill_count: 0
    .wavefront_size: 64
  - .agpr_count:     0
    .args:
      - .actual_access:  read_only
        .address_space:  global
        .offset:         0
        .size:           8
        .value_kind:     global_buffer
      - .actual_access:  read_only
        .address_space:  global
        .offset:         8
        .size:           8
        .value_kind:     global_buffer
      - .actual_access:  read_only
        .address_space:  global
        .offset:         16
        .size:           8
        .value_kind:     global_buffer
      - .actual_access:  read_only
        .address_space:  global
        .offset:         24
        .size:           8
        .value_kind:     global_buffer
      - .actual_access:  read_only
        .address_space:  global
        .offset:         32
        .size:           8
        .value_kind:     global_buffer
      - .actual_access:  read_only
        .address_space:  global
        .offset:         40
        .size:           8
        .value_kind:     global_buffer
      - .actual_access:  read_only
        .address_space:  global
        .offset:         48
        .size:           8
        .value_kind:     global_buffer
      - .actual_access:  write_only
        .address_space:  global
        .offset:         56
        .size:           8
        .value_kind:     global_buffer
      - .actual_access:  write_only
        .address_space:  global
        .offset:         64
        .size:           8
        .value_kind:     global_buffer
      - .actual_access:  write_only
        .address_space:  global
        .offset:         72
        .size:           8
        .value_kind:     global_buffer
      - .actual_access:  read_only
        .address_space:  global
        .offset:         80
        .size:           8
        .value_kind:     global_buffer
      - .actual_access:  read_only
        .address_space:  global
        .offset:         88
        .size:           8
        .value_kind:     global_buffer
      - .actual_access:  write_only
        .address_space:  global
        .offset:         96
        .size:           8
        .value_kind:     global_buffer
      - .actual_access:  write_only
        .address_space:  global
        .offset:         104
        .size:           8
        .value_kind:     global_buffer
    .group_segment_fixed_size: 30768
    .kernarg_segment_align: 8
    .kernarg_segment_size: 112
    .language:       OpenCL C
    .language_version:
      - 2
      - 0
    .max_flat_workgroup_size: 512
    .name:           _Z7k_fine3PKfS0_PKtS2_PKdS4_S0_PiPfS5_S0_S0_PtS7_
    .private_segment_fixed_size: 0
    .sgpr_count:     106
    .sgpr_spill_count: 4
    .symbol:         _Z7k_fine3PKfS0_PKtS2_PKdS4_S0_PiPfS5_S0_S0_PtS7_.kd
    .uniform_work_group_size: 1
    .uses_dynamic_stack: false
    .vgpr_count:     256
    .vgpr_spill_count: 0
    .wavefront_size: 64
  - .agpr_count:     0
    .args:
      - .actual_access:  read_only
        .address_space:  global
        .offset:         0
        .size:           8
        .value_kind:     global_buffer
      - .actual_access:  read_only
        .address_space:  global
        .offset:         8
        .size:           8
        .value_kind:     global_buffer
      - .actual_access:  read_only
        .address_space:  global
        .offset:         16
        .size:           8
        .value_kind:     global_buffer
      - .actual_access:  read_only
        .address_space:  global
        .offset:         24
        .size:           8
        .value_kind:     global_buffer
      - .actual_access:  read_only
        .address_space:  global
        .offset:         32
        .size:           8
        .value_kind:     global_buffer
      - .actual_access:  read_only
        .address_space:  global
        .offset:         40
        .size:           8
        .value_kind:     global_buffer
      - .actual_access:  write_only
        .address_space:  global
        .offset:         48
        .size:           8
        .value_kind:     global_buffer
      - .actual_access:  write_only
        .address_space:  global
        .offset:         56
        .size:           8
        .value_kind:     global_buffer
      - .actual_access:  write_only
        .address_space:  global
        .offset:         64
        .size:           8
        .value_kind:     global_buffer
    .group_segment_fixed_size: 18512
    .kernarg_segment_align: 8
    .kernarg_segment_size: 72
    .language:       OpenCL C
    .language_version:
      - 2
      - 0
    .max_flat_workgroup_size: 256
    .name:           _Z10k_transferPKtS0_PKfPKiS2_S4_PfS5_S5_
    .private_segment_fixed_size: 0
    .sgpr_count:     34
    .sgpr_spill_count: 0
    .symbol:         _Z10k_transferPKtS0_PKfPKiS2_S4_PfS5_S5_.kd
    .uniform_work_group_size: 1
    .uses_dynamic_stack: false
    .vgpr_count:     49
    .vgpr_spill_count: 0
    .wavefront_size: 64
